# speedup vs baseline: 1.0028x; 1.0010x over previous
.LBB5_12:
	s_or_b64 exec, exec, s[0:1]
	s_lshl_b32 s0, s42, 9
	s_ashr_i32 s1, s0, 31
	s_lshl_b64 s[0:1], s[0:1], 2
	s_add_u32 s0, s24, s0
	s_addc_u32 s1, s25, s1
	s_lshl_b32 s2, s7, 2
	v_bfe_u32 v153, v0, 6, 2
	s_add_u32 s0, s0, s2
	s_addc_u32 s1, s1, 0
	v_lshlrev_b32_e32 v148, 7, v153
	v_mov_b32_e32 v149, 0
	v_lshl_add_u64 v[10:11], s[0:1], 0, v[148:149]
	v_mov_b32_e32 v147, v149
	v_lshl_add_u64 v[10:11], v[10:11], 0, v[146:147]
	v_and_b32_e32 v254, 48, v0
	v_lshl_add_u32 v254, v153, 7, v254
	v_add_u32_e32 v254, 0x22240, v254
	ds_read_b128 v[34:37], v254
	ds_read_b128 v[26:29], v254 offset:64
	ds_read_b128 v[18:21], v254 offset:512
	ds_read_b128 v[10:13], v254 offset:576
	s_ashr_i32 s35, s34, 31
	s_and_b32 s50, s59, 6
	s_lshl_b64 s[2:3], s[34:35], 3
	s_or_b32 s7, s2, s50
	s_or_b32 s2, s7, s58
	s_lshl_b64 s[24:25], s[2:3], 16
	v_lshrrev_b32_e32 v187, 6, v0
	s_add_u32 s28, s26, s24
	v_and_b32_e32 v157, 4, v187
	s_addc_u32 s29, s27, s25
	s_lshl_b32 s2, s58, 3
	v_lshlrev_b32_e32 v147, 6, v188
	v_lshrrev_b32_e32 v148, 1, v0
	v_lshlrev_b32_e32 v154, 10, v153
	v_lshlrev_b32_e32 v158, 13, v157
	s_cmp_lg_u32 s58, 0
	v_lshl_or_b32 v159, v157, 4, s2
	v_and_or_b32 v155, v148, 24, v147
	v_or_b32_e32 v148, v154, v158
	s_cselect_b64 s[24:25], -1, 0
	v_or_b32_e32 v156, v153, v159
	s_mov_b64 s[0:1], -1
	v_lshl_add_u64 v[150:151], s[28:29], 0, v[148:149]
	v_or_b32_e32 v148, v155, v152
	v_lshl_add_u32 v156, v156, 10, 0
	s_and_b64 vcc, exec, s[24:25]
	s_waitcnt vmcnt(0) lgkmcnt(0)
	s_barrier
	v_lshrrev_b32_e32 v250, 6, v0
	v_and_b32_e32 v251, 63, v0
	s_lshl_b32 s96, s42, 3
	v_or_b32_e32 v250, s96, v250
	v_lshlrev_b32_e32 v250, 16, v250
	v_lshl_add_u32 v250, v251, 4, v250
	s_lshl_b32 s96, s58, 3
	s_and_b32 s97, s33, 6
	s_or_b32 s96, s96, s97
	s_lshl_b32 s96, s96, 12
	s_add_u32 s96, s48, s96
	s_addc_u32 s97, s49, 0
	global_load_dwordx4 v[200:203], v250, s[96:97]
	global_load_dwordx4 v[204:207], v250, s[96:97] offset:1024
	global_load_dwordx4 v[208:211], v250, s[96:97] offset:2048
	global_load_dwordx4 v[212:215], v250, s[96:97] offset:3072
	s_add_u32 s96, s96, 0x1000
	s_addc_u32 s97, s97, 0
	global_load_dwordx4 v[216:219], v250, s[96:97]
	global_load_dwordx4 v[220:223], v250, s[96:97] offset:1024
	global_load_dwordx4 v[224:227], v250, s[96:97] offset:2048
	global_load_dwordx4 v[228:231], v250, s[96:97] offset:3072
	v_fmamk_f32 v142, v142, 0x3c800000, v34
	v_fmamk_f32 v143, v143, 0x3c800000, v35
	v_fmamk_f32 v144, v144, 0x3c800000, v36
	v_fmamk_f32 v145, v145, 0x3c800000, v37
	v_max_f32_e32 v142, 0, v142
	v_max_f32_e32 v160, 0, v143
	v_max_f32_e32 v143, 0, v144
	v_max_f32_e32 v144, 0, v145
	v_cvt_pk_f16_f32 v143, v143, v144
	v_cvt_pk_f16_f32 v142, v142, v160
	s_cbranch_vccz .LBB5_14
	v_lshl_add_u64 v[144:145], v[150:151], 0, v[148:149]
	global_store_dwordx2 v[144:145], v[142:143], off sc1
	s_mov_b64 s[0:1], 0

.LBB5_140:
	v_lshl_or_b32 v2, s42, 3, v187
	v_ashrrev_i32_e32 v3, 31, v2
	v_lshlrev_b64 v[2:3], 16, v[2:3]
	v_lshl_add_u64 v[2:3], s[48:49], 0, v[2:3]
	v_mov_b32_e32 v169, 0
	v_lshlrev_b32_e32 v168, 4, v189
	s_or_b32 s25, s2, s50
	s_or_b32 s24, s50, 1
	s_mov_b32 s1, 0
	v_lshl_add_u64 v[166:167], v[2:3], 0, v[168:169]
	s_lshl_b32 s0, s25, 12
	s_or_b32 s30, s2, s24
	v_lshl_add_u64 v[18:19], v[166:167], 0, s[0:1]
	s_lshl_b32 s0, s30, 12
	v_lshl_add_u64 v[34:35], v[166:167], 0, s[0:1]
	s_waitcnt vmcnt(16)
	v_mov_b32_e32 v2, v200
	v_mov_b32_e32 v3, v201
	v_mov_b32_e32 v4, v202
	v_mov_b32_e32 v5, v203
	v_mov_b32_e32 v6, v204
	v_mov_b32_e32 v7, v205
	v_mov_b32_e32 v8, v206
	v_mov_b32_e32 v9, v207
	v_mov_b32_e32 v10, v208
	v_mov_b32_e32 v11, v209
	v_mov_b32_e32 v12, v210
	v_mov_b32_e32 v13, v211
	v_mov_b32_e32 v14, v212
	v_mov_b32_e32 v15, v213
	v_mov_b32_e32 v16, v214
	v_mov_b32_e32 v17, v215
	v_mov_b32_e32 v18, v216
	v_mov_b32_e32 v19, v217
	v_mov_b32_e32 v20, v218
	v_mov_b32_e32 v21, v219
	v_mov_b32_e32 v22, v220
	v_mov_b32_e32 v23, v221
	v_mov_b32_e32 v24, v222
	v_mov_b32_e32 v25, v223
	v_mov_b32_e32 v26, v224
	v_mov_b32_e32 v27, v225
	v_mov_b32_e32 v28, v226
	v_mov_b32_e32 v29, v227
	v_mov_b32_e32 v30, v228
	v_mov_b32_e32 v31, v229
	v_mov_b32_e32 v32, v230
	v_mov_b32_e32 v33, v231
	v_or_b32_e32 v52, v147, v146
	s_add_i32 s0, s59, 2
	s_and_b32 s28, s0, 6
	s_or_b32 s31, s2, s28
	s_lshl_b32 s0, s31, 12
	v_lshl_add_u64 v[50:51], v[166:167], 0, s[0:1]
	s_waitcnt lgkmcnt(0)
	s_barrier
	global_load_dwordx4 v[34:37], v[50:51], off
	global_load_dwordx4 v[38:41], v[50:51], off offset:1024
	global_load_dwordx4 v[42:45], v[50:51], off offset:2048
	global_load_dwordx4 v[46:49], v[50:51], off offset:3072
	v_xad_u32 v191, v52, v152, 0
	v_lshl_add_u32 v122, s25, 10, v191
	ds_read_b128 v[50:53], v122
	ds_read_b128 v[54:57], v122 offset:16384
	ds_read_b128 v[58:61], v122 offset:32768
	ds_read_b128 v[62:65], v122 offset:49152
	s_setprio 1
	s_waitcnt vmcnt(27) lgkmcnt(3)
	v_mfma_f32_16x16x32_f16 v[66:69], v[2:5], v[50:53], 0
	s_waitcnt vmcnt(26)
	v_mfma_f32_16x16x32_f16 v[70:73], v[6:9], v[50:53], 0
	s_waitcnt vmcnt(25)
	v_mfma_f32_16x16x32_f16 v[74:77], v[10:13], v[50:53], 0
	s_waitcnt vmcnt(24)
	v_mfma_f32_16x16x32_f16 v[50:53], v[14:17], v[50:53], 0
	s_waitcnt lgkmcnt(2)
	v_mfma_f32_16x16x32_f16 v[78:81], v[2:5], v[54:57], 0
	v_mfma_f32_16x16x32_f16 v[82:85], v[6:9], v[54:57], 0
	v_mfma_f32_16x16x32_f16 v[86:89], v[10:13], v[54:57], 0
	v_mfma_f32_16x16x32_f16 v[54:57], v[14:17], v[54:57], 0
	s_waitcnt lgkmcnt(1)
	v_mfma_f32_16x16x32_f16 v[90:93], v[2:5], v[58:61], 0
	v_mfma_f32_16x16x32_f16 v[94:97], v[6:9], v[58:61], 0
	v_mfma_f32_16x16x32_f16 v[98:101], v[10:13], v[58:61], 0
	v_mfma_f32_16x16x32_f16 v[58:61], v[14:17], v[58:61], 0
	s_waitcnt lgkmcnt(0)
	v_mfma_f32_16x16x32_f16 v[102:105], v[2:5], v[62:65], 0
	v_mfma_f32_16x16x32_f16 v[106:109], v[6:9], v[62:65], 0
	v_mfma_f32_16x16x32_f16 v[110:113], v[10:13], v[62:65], 0
	v_mfma_f32_16x16x32_f16 v[62:65], v[14:17], v[62:65], 0
	s_setprio 0
	v_add_u32_e32 v114, 0x10000, v122
	v_add_u32_e32 v118, 0x14000, v122
	v_add_u32_e32 v123, 0x18000, v122
	v_add_u32_e32 v126, 0x1c000, v122
	ds_read_b128 v[114:117], v114
	ds_read_b128 v[118:121], v118
	ds_read_b128 v[122:125], v123
	ds_read_b128 v[126:129], v126
	s_setprio 1
	s_waitcnt lgkmcnt(3)
	v_mfma_f32_16x16x32_f16 v[130:133], v[2:5], v[114:117], 0
	v_mfma_f32_16x16x32_f16 v[134:137], v[6:9], v[114:117], 0
	v_mfma_f32_16x16x32_f16 v[138:141], v[10:13], v[114:117], 0
	v_mfma_f32_16x16x32_f16 v[114:117], v[14:17], v[114:117], 0
	s_waitcnt lgkmcnt(2)
	v_mfma_f32_16x16x32_f16 v[142:145], v[2:5], v[118:121], 0
	v_mfma_f32_16x16x32_f16 v[146:149], v[6:9], v[118:121], 0
	v_mfma_f32_16x16x32_f16 v[150:153], v[10:13], v[118:121], 0
	v_mfma_f32_16x16x32_f16 v[118:121], v[14:17], v[118:121], 0
	s_waitcnt lgkmcnt(1)
	v_mfma_f32_16x16x32_f16 v[154:157], v[2:5], v[122:125], 0
	v_mfma_f32_16x16x32_f16 v[158:161], v[6:9], v[122:125], 0
	v_mfma_f32_16x16x32_f16 v[170:173], v[10:13], v[122:125], 0
	v_mfma_f32_16x16x32_f16 v[122:125], v[14:17], v[122:125], 0
	s_waitcnt lgkmcnt(0)
	v_mfma_f32_16x16x32_f16 v[2:5], v[2:5], v[126:129], 0
	v_mfma_f32_16x16x32_f16 v[6:9], v[6:9], v[126:129], 0
	v_mfma_f32_16x16x32_f16 v[10:13], v[10:13], v[126:129], 0
	v_mfma_f32_16x16x32_f16 v[14:17], v[14:17], v[126:129], 0
	s_setprio 0
	s_add_i32 s0, s50, 3
	s_and_b32 s29, s0, 7
	s_or_b32 s48, s29, s2
	s_lshl_b32 s0, s48, 12
	v_lshl_add_u64 v[178:179], v[166:167], 0, s[0:1]
	global_load_dwordx4 v[126:129], v[178:179], off
	global_load_dwordx4 v[174:177], v[178:179], off offset:1024
	global_load_dwordx4 v[192:195], v[178:179], off offset:2048
	global_load_dwordx4 v[196:199], v[178:179], off offset:3072
	v_lshl_add_u32 v163, s30, 10, v191
	ds_read_b128 v[200:203], v163
	ds_read_b128 v[204:207], v163 offset:16384
	ds_read_b128 v[208:211], v163 offset:32768
	ds_read_b128 v[212:215], v163 offset:49152
	s_setprio 1
	s_waitcnt vmcnt(27) lgkmcnt(3)
	v_mfma_f32_16x16x32_f16 v[66:69], v[18:21], v[200:203], v[66:69]
	s_waitcnt vmcnt(26)
	v_mfma_f32_16x16x32_f16 v[70:73], v[22:25], v[200:203], v[70:73]
	s_waitcnt vmcnt(25)
	v_mfma_f32_16x16x32_f16 v[74:77], v[26:29], v[200:203], v[74:77]
	s_waitcnt vmcnt(24)
	v_mfma_f32_16x16x32_f16 v[50:53], v[30:33], v[200:203], v[50:53]
	s_waitcnt lgkmcnt(2)
	v_mfma_f32_16x16x32_f16 v[78:81], v[18:21], v[204:207], v[78:81]
	v_mfma_f32_16x16x32_f16 v[82:85], v[22:25], v[204:207], v[82:85]
	v_mfma_f32_16x16x32_f16 v[86:89], v[26:29], v[204:207], v[86:89]
	v_mfma_f32_16x16x32_f16 v[54:57], v[30:33], v[204:207], v[54:57]
	s_waitcnt lgkmcnt(1)
	v_mfma_f32_16x16x32_f16 v[90:93], v[18:21], v[208:211], v[90:93]
	v_mfma_f32_16x16x32_f16 v[94:97], v[22:25], v[208:211], v[94:97]
	v_mfma_f32_16x16x32_f16 v[98:101], v[26:29], v[208:211], v[98:101]
	v_mfma_f32_16x16x32_f16 v[58:61], v[30:33], v[208:211], v[58:61]
	s_waitcnt lgkmcnt(0)
	v_mfma_f32_16x16x32_f16 v[102:105], v[18:21], v[212:215], v[102:105]
	v_mfma_f32_16x16x32_f16 v[106:109], v[22:25], v[212:215], v[106:109]
	v_mfma_f32_16x16x32_f16 v[110:113], v[26:29], v[212:215], v[110:113]
	v_mfma_f32_16x16x32_f16 v[62:65], v[30:33], v[212:215], v[62:65]
	s_setprio 0
	v_add_u32_e32 v165, 0x10000, v163
	v_add_u32_e32 v168, 0x14000, v163
	ds_read_b128 v[200:203], v165
	ds_read_b128 v[204:207], v168
	v_add_u32_e32 v165, 0x18000, v163
	v_add_u32_e32 v163, 0x1c000, v163
	ds_read_b128 v[208:211], v165
	ds_read_b128 v[212:215], v163
	s_setprio 1
	s_waitcnt lgkmcnt(3)
	v_mfma_f32_16x16x32_f16 v[130:133], v[18:21], v[200:203], v[130:133]
	v_mfma_f32_16x16x32_f16 v[134:137], v[22:25], v[200:203], v[134:137]
	v_mfma_f32_16x16x32_f16 v[138:141], v[26:29], v[200:203], v[138:141]
	v_mfma_f32_16x16x32_f16 v[114:117], v[30:33], v[200:203], v[114:117]
	s_waitcnt lgkmcnt(2)
	v_mfma_f32_16x16x32_f16 v[142:145], v[18:21], v[204:207], v[142:145]
	v_mfma_f32_16x16x32_f16 v[146:149], v[22:25], v[204:207], v[146:149]
	v_mfma_f32_16x16x32_f16 v[150:153], v[26:29], v[204:207], v[150:153]
	v_mfma_f32_16x16x32_f16 v[118:121], v[30:33], v[204:207], v[118:121]
	s_waitcnt lgkmcnt(1)
	v_mfma_f32_16x16x32_f16 v[154:157], v[18:21], v[208:211], v[154:157]
	v_mfma_f32_16x16x32_f16 v[158:161], v[22:25], v[208:211], v[158:161]
	v_mfma_f32_16x16x32_f16 v[122:125], v[30:33], v[208:211], v[122:125]
	s_waitcnt lgkmcnt(0)
	v_mfma_f32_16x16x32_f16 v[2:5], v[18:21], v[212:215], v[2:5]
	v_mfma_f32_16x16x32_f16 v[6:9], v[22:25], v[212:215], v[6:9]
	v_mfma_f32_16x16x32_f16 v[10:13], v[26:29], v[212:215], v[10:13]
	v_mfma_f32_16x16x32_f16 v[14:17], v[30:33], v[212:215], v[14:17]
	v_mfma_f32_16x16x32_f16 v[170:173], v[26:29], v[208:211], v[170:173]
	s_setprio 0
	s_xor_b32 s25, s25, 4
	s_lshl_b32 s0, s25, 12
	v_lshl_add_u64 v[30:31], v[166:167], 0, s[0:1]
	s_waitcnt vmcnt(8)
	s_barrier
	s_getreg_b32 s80, hwreg(HW_REG_XCC_ID, 0, 4)
	s_and_b32 s80, s80, 15
	s_add_i32 s80, s80, 1
	s_lshl_b32 s81, s34, 3
	s_or_b32 s81, s81, s33
	s_lshl_b32 s81, s81, 7
	s_add_u32 s82, s46, s81
	s_addc_u32 s83, s47, 0
	v_mov_b32_e32 v254, 0
	v_mov_b32_e32 v255, s80
	s_and_saveexec_b64 s[84:85], s[4:5]
	global_store_dword v254, v255, s[82:83] sc1
	s_mov_b64 exec, s[84:85]
	global_load_dwordx4 v[18:21], v[30:31], off
	global_load_dwordx4 v[22:25], v[30:31], off offset:1024
	global_load_dwordx4 v[26:29], v[30:31], off offset:2048
	s_nop 0
	global_load_dwordx4 v[30:33], v[30:31], off offset:3072
	v_lshl_add_u32 v163, s31, 10, v191
	ds_read_b128 v[200:203], v163
	ds_read_b128 v[204:207], v163 offset:16384
	ds_read_b128 v[208:211], v163 offset:32768
	ds_read_b128 v[212:215], v163 offset:49152
	s_setprio 1
	s_waitcnt vmcnt(11) lgkmcnt(3)
	v_mfma_f32_16x16x32_f16 v[66:69], v[34:37], v[200:203], v[66:69]
	s_waitcnt vmcnt(10)
	v_mfma_f32_16x16x32_f16 v[70:73], v[38:41], v[200:203], v[70:73]
	s_waitcnt vmcnt(9)
	v_mfma_f32_16x16x32_f16 v[74:77], v[42:45], v[200:203], v[74:77]
	s_waitcnt vmcnt(8)
	v_mfma_f32_16x16x32_f16 v[50:53], v[46:49], v[200:203], v[50:53]
	s_waitcnt lgkmcnt(2)
	v_mfma_f32_16x16x32_f16 v[78:81], v[34:37], v[204:207], v[78:81]
	v_mfma_f32_16x16x32_f16 v[82:85], v[38:41], v[204:207], v[82:85]
	v_mfma_f32_16x16x32_f16 v[86:89], v[42:45], v[204:207], v[86:89]
	v_mfma_f32_16x16x32_f16 v[54:57], v[46:49], v[204:207], v[54:57]
	s_waitcnt lgkmcnt(1)
	v_mfma_f32_16x16x32_f16 v[90:93], v[34:37], v[208:211], v[90:93]
	v_mfma_f32_16x16x32_f16 v[94:97], v[38:41], v[208:211], v[94:97]
	v_mfma_f32_16x16x32_f16 v[98:101], v[42:45], v[208:211], v[98:101]
	v_mfma_f32_16x16x32_f16 v[58:61], v[46:49], v[208:211], v[58:61]
	s_waitcnt lgkmcnt(0)
	v_mfma_f32_16x16x32_f16 v[102:105], v[34:37], v[212:215], v[102:105]
	v_mfma_f32_16x16x32_f16 v[106:109], v[38:41], v[212:215], v[106:109]
	v_mfma_f32_16x16x32_f16 v[110:113], v[42:45], v[212:215], v[110:113]
	v_mfma_f32_16x16x32_f16 v[62:65], v[46:49], v[212:215], v[62:65]
	s_setprio 0
	v_add_u32_e32 v165, 0x10000, v163
	v_add_u32_e32 v168, 0x14000, v163
	ds_read_b128 v[200:203], v165
	ds_read_b128 v[204:207], v168
	v_add_u32_e32 v165, 0x18000, v163
	v_add_u32_e32 v163, 0x1c000, v163
	ds_read_b128 v[208:211], v165
	ds_read_b128 v[212:215], v163
	s_setprio 1
	s_waitcnt lgkmcnt(3)
	v_mfma_f32_16x16x32_f16 v[130:133], v[34:37], v[200:203], v[130:133]
	v_mfma_f32_16x16x32_f16 v[134:137], v[38:41], v[200:203], v[134:137]
	v_mfma_f32_16x16x32_f16 v[138:141], v[42:45], v[200:203], v[138:141]
	v_mfma_f32_16x16x32_f16 v[114:117], v[46:49], v[200:203], v[114:117]
	s_waitcnt lgkmcnt(2)
	v_mfma_f32_16x16x32_f16 v[142:145], v[34:37], v[204:207], v[142:145]
	v_mfma_f32_16x16x32_f16 v[146:149], v[38:41], v[204:207], v[146:149]
	v_mfma_f32_16x16x32_f16 v[150:153], v[42:45], v[204:207], v[150:153]
	v_mfma_f32_16x16x32_f16 v[118:121], v[46:49], v[204:207], v[118:121]
	s_waitcnt lgkmcnt(1)
	v_mfma_f32_16x16x32_f16 v[154:157], v[34:37], v[208:211], v[154:157]
	v_mfma_f32_16x16x32_f16 v[158:161], v[38:41], v[208:211], v[158:161]
	v_mfma_f32_16x16x32_f16 v[122:125], v[46:49], v[208:211], v[122:125]
	s_waitcnt lgkmcnt(0)
	v_mfma_f32_16x16x32_f16 v[2:5], v[34:37], v[212:215], v[2:5]
	v_mfma_f32_16x16x32_f16 v[6:9], v[38:41], v[212:215], v[6:9]
	v_mfma_f32_16x16x32_f16 v[10:13], v[42:45], v[212:215], v[10:13]
	v_mfma_f32_16x16x32_f16 v[14:17], v[46:49], v[212:215], v[14:17]
	v_mfma_f32_16x16x32_f16 v[170:173], v[42:45], v[208:211], v[170:173]
	s_setprio 0
	s_add_i32 s0, s50, 5
	s_and_b32 s30, s0, 7
	s_or_b32 s49, s30, s2
	s_lshl_b32 s0, s49, 12
	v_lshl_add_u64 v[46:47], v[166:167], 0, s[0:1]
	global_load_dwordx4 v[34:37], v[46:47], off
	global_load_dwordx4 v[38:41], v[46:47], off offset:1024
	global_load_dwordx4 v[42:45], v[46:47], off offset:2048
	s_nop 0
	global_load_dwordx4 v[46:49], v[46:47], off offset:3072
	v_lshl_add_u32 v163, s48, 10, v191
	ds_read_b128 v[200:203], v163
	ds_read_b128 v[204:207], v163 offset:16384
	ds_read_b128 v[208:211], v163 offset:32768
	ds_read_b128 v[212:215], v163 offset:49152
	s_setprio 1
	s_waitcnt vmcnt(11) lgkmcnt(3)
	v_mfma_f32_16x16x32_f16 v[66:69], v[126:129], v[200:203], v[66:69]
	s_waitcnt vmcnt(10)
	v_mfma_f32_16x16x32_f16 v[70:73], v[174:177], v[200:203], v[70:73]
	s_waitcnt vmcnt(9)
	v_mfma_f32_16x16x32_f16 v[74:77], v[192:195], v[200:203], v[74:77]
	s_waitcnt vmcnt(8)
	v_mfma_f32_16x16x32_f16 v[50:53], v[196:199], v[200:203], v[50:53]
	s_waitcnt lgkmcnt(2)
	v_mfma_f32_16x16x32_f16 v[78:81], v[126:129], v[204:207], v[78:81]
	v_mfma_f32_16x16x32_f16 v[82:85], v[174:177], v[204:207], v[82:85]
	v_mfma_f32_16x16x32_f16 v[86:89], v[192:195], v[204:207], v[86:89]
	v_mfma_f32_16x16x32_f16 v[54:57], v[196:199], v[204:207], v[54:57]
	s_waitcnt lgkmcnt(1)
	v_mfma_f32_16x16x32_f16 v[90:93], v[126:129], v[208:211], v[90:93]
	v_mfma_f32_16x16x32_f16 v[94:97], v[174:177], v[208:211], v[94:97]
	v_mfma_f32_16x16x32_f16 v[98:101], v[192:195], v[208:211], v[98:101]
	v_mfma_f32_16x16x32_f16 v[58:61], v[196:199], v[208:211], v[58:61]
	s_waitcnt lgkmcnt(0)
	v_mfma_f32_16x16x32_f16 v[102:105], v[126:129], v[212:215], v[102:105]
	v_mfma_f32_16x16x32_f16 v[106:109], v[174:177], v[212:215], v[106:109]
	v_mfma_f32_16x16x32_f16 v[110:113], v[192:195], v[212:215], v[110:113]
	v_mfma_f32_16x16x32_f16 v[62:65], v[196:199], v[212:215], v[62:65]
	s_setprio 0
	v_add_u32_e32 v165, 0x10000, v163
	v_add_u32_e32 v168, 0x14000, v163
	ds_read_b128 v[200:203], v165
	ds_read_b128 v[204:207], v168
	v_add_u32_e32 v165, 0x18000, v163
	v_add_u32_e32 v163, 0x1c000, v163
	ds_read_b128 v[208:211], v165
	ds_read_b128 v[212:215], v163
	s_setprio 1
	s_waitcnt lgkmcnt(3)
	v_mfma_f32_16x16x32_f16 v[130:133], v[126:129], v[200:203], v[130:133]
	v_mfma_f32_16x16x32_f16 v[134:137], v[174:177], v[200:203], v[134:137]
	v_mfma_f32_16x16x32_f16 v[138:141], v[192:195], v[200:203], v[138:141]
	v_mfma_f32_16x16x32_f16 v[114:117], v[196:199], v[200:203], v[114:117]
	s_waitcnt lgkmcnt(2)
	v_mfma_f32_16x16x32_f16 v[142:145], v[126:129], v[204:207], v[142:145]
	v_mfma_f32_16x16x32_f16 v[146:149], v[174:177], v[204:207], v[146:149]
	v_mfma_f32_16x16x32_f16 v[150:153], v[192:195], v[204:207], v[150:153]
	v_mfma_f32_16x16x32_f16 v[118:121], v[196:199], v[204:207], v[118:121]
	s_waitcnt lgkmcnt(1)
	v_mfma_f32_16x16x32_f16 v[154:157], v[126:129], v[208:211], v[154:157]
	v_mfma_f32_16x16x32_f16 v[158:161], v[174:177], v[208:211], v[158:161]
	v_mfma_f32_16x16x32_f16 v[122:125], v[196:199], v[208:211], v[122:125]
	s_waitcnt lgkmcnt(0)
	v_mfma_f32_16x16x32_f16 v[2:5], v[126:129], v[212:215], v[2:5]
	v_mfma_f32_16x16x32_f16 v[6:9], v[174:177], v[212:215], v[6:9]
	v_mfma_f32_16x16x32_f16 v[10:13], v[192:195], v[212:215], v[10:13]
	v_mfma_f32_16x16x32_f16 v[14:17], v[196:199], v[212:215], v[14:17]
	v_mfma_f32_16x16x32_f16 v[170:173], v[192:195], v[208:211], v[170:173]
	s_setprio 0
	s_add_i32 s59, s59, 6
	s_and_b32 s31, s59, 6
	s_or_b32 s52, s2, s31
	s_lshl_b32 s0, s52, 12
	v_lshl_add_u64 v[178:179], v[166:167], 0, s[0:1]
	s_lshl_b32 s86, s34, 3
	s_or_b32 s86, s86, s33
	s_xor_b32 s86, s86, 1
	s_lshl_b32 s86, s86, 7
	s_add_u32 s86, s46, s86
	s_addc_u32 s87, s47, 0
	v_mov_b32_e32 v254, 0
	global_load_dword v254, v254, s[86:87] sc1
	global_load_dwordx4 v[126:129], v[178:179], off
	global_load_dwordx4 v[174:177], v[178:179], off offset:1024
	global_load_dwordx4 v[192:195], v[178:179], off offset:2048
	global_load_dwordx4 v[196:199], v[178:179], off offset:3072
	v_lshl_add_u32 v163, s25, 10, v191
	ds_read_b128 v[200:203], v163
	ds_read_b128 v[204:207], v163 offset:16384
	ds_read_b128 v[208:211], v163 offset:32768
	ds_read_b128 v[212:215], v163 offset:49152
	s_setprio 1
	s_waitcnt vmcnt(12) lgkmcnt(3)
	v_mfma_f32_16x16x32_f16 v[66:69], v[18:21], v[200:203], v[66:69]
	s_waitcnt vmcnt(11)
	v_mfma_f32_16x16x32_f16 v[70:73], v[22:25], v[200:203], v[70:73]
	s_waitcnt vmcnt(10)
	v_mfma_f32_16x16x32_f16 v[74:77], v[26:29], v[200:203], v[74:77]
	s_waitcnt vmcnt(9)
	v_mfma_f32_16x16x32_f16 v[50:53], v[30:33], v[200:203], v[50:53]
	s_waitcnt lgkmcnt(2)
	v_mfma_f32_16x16x32_f16 v[78:81], v[18:21], v[204:207], v[78:81]
	v_mfma_f32_16x16x32_f16 v[82:85], v[22:25], v[204:207], v[82:85]
	v_mfma_f32_16x16x32_f16 v[86:89], v[26:29], v[204:207], v[86:89]
	v_mfma_f32_16x16x32_f16 v[54:57], v[30:33], v[204:207], v[54:57]
	s_waitcnt lgkmcnt(1)
	v_mfma_f32_16x16x32_f16 v[90:93], v[18:21], v[208:211], v[90:93]
	v_mfma_f32_16x16x32_f16 v[94:97], v[22:25], v[208:211], v[94:97]
	v_mfma_f32_16x16x32_f16 v[98:101], v[26:29], v[208:211], v[98:101]
	v_mfma_f32_16x16x32_f16 v[58:61], v[30:33], v[208:211], v[58:61]
	s_waitcnt lgkmcnt(0)
	v_mfma_f32_16x16x32_f16 v[102:105], v[18:21], v[212:215], v[102:105]
	v_mfma_f32_16x16x32_f16 v[106:109], v[22:25], v[212:215], v[106:109]
	v_mfma_f32_16x16x32_f16 v[110:113], v[26:29], v[212:215], v[110:113]
	v_mfma_f32_16x16x32_f16 v[62:65], v[30:33], v[212:215], v[62:65]
	s_setprio 0
	v_add_u32_e32 v165, 0x10000, v163
	v_add_u32_e32 v168, 0x14000, v163
	ds_read_b128 v[200:203], v165
	ds_read_b128 v[204:207], v168
	v_add_u32_e32 v165, 0x18000, v163
	v_add_u32_e32 v163, 0x1c000, v163
	ds_read_b128 v[208:211], v165
	ds_read_b128 v[212:215], v163
	s_setprio 1
	s_waitcnt lgkmcnt(3)
	v_mfma_f32_16x16x32_f16 v[130:133], v[18:21], v[200:203], v[130:133]
	v_mfma_f32_16x16x32_f16 v[134:137], v[22:25], v[200:203], v[134:137]
	v_mfma_f32_16x16x32_f16 v[138:141], v[26:29], v[200:203], v[138:141]
	v_mfma_f32_16x16x32_f16 v[114:117], v[30:33], v[200:203], v[114:117]
	s_waitcnt lgkmcnt(2)
	v_mfma_f32_16x16x32_f16 v[142:145], v[18:21], v[204:207], v[142:145]
	v_mfma_f32_16x16x32_f16 v[146:149], v[22:25], v[204:207], v[146:149]
	v_mfma_f32_16x16x32_f16 v[150:153], v[26:29], v[204:207], v[150:153]
	v_mfma_f32_16x16x32_f16 v[118:121], v[30:33], v[204:207], v[118:121]
	s_waitcnt lgkmcnt(1)
	v_mfma_f32_16x16x32_f16 v[154:157], v[18:21], v[208:211], v[154:157]
	v_mfma_f32_16x16x32_f16 v[158:161], v[22:25], v[208:211], v[158:161]
	v_mfma_f32_16x16x32_f16 v[122:125], v[30:33], v[208:211], v[122:125]
	s_waitcnt lgkmcnt(0)
	v_mfma_f32_16x16x32_f16 v[2:5], v[18:21], v[212:215], v[2:5]
	v_mfma_f32_16x16x32_f16 v[6:9], v[22:25], v[212:215], v[6:9]
	v_mfma_f32_16x16x32_f16 v[10:13], v[26:29], v[212:215], v[10:13]
	v_mfma_f32_16x16x32_f16 v[14:17], v[30:33], v[212:215], v[14:17]
	v_mfma_f32_16x16x32_f16 v[170:173], v[26:29], v[208:211], v[170:173]
	s_setprio 0
	s_add_i32 s0, s50, -1
	s_and_b32 s48, s0, 7
	s_or_b32 s25, s48, s2
	s_lshl_b32 s0, s25, 12
	v_lshl_add_u64 v[18:19], v[166:167], 0, s[0:1]
	global_load_dwordx4 v[200:203], v[18:19], off
	global_load_dwordx4 v[204:207], v[18:19], off offset:1024
	global_load_dwordx4 v[208:211], v[18:19], off offset:2048
	global_load_dwordx4 v[212:215], v[18:19], off offset:3072
	v_lshl_add_u32 v163, s49, 10, v191
	ds_read_b128 v[18:21], v163
	ds_read_b128 v[22:25], v163 offset:16384
	ds_read_b128 v[26:29], v163 offset:32768
	ds_read_b128 v[30:33], v163 offset:49152
	s_setprio 1
	s_waitcnt vmcnt(12) lgkmcnt(3)
	v_mfma_f32_16x16x32_f16 v[66:69], v[34:37], v[18:21], v[66:69]
	s_waitcnt vmcnt(11)
	v_mfma_f32_16x16x32_f16 v[70:73], v[38:41], v[18:21], v[70:73]
	s_waitcnt vmcnt(10)
	v_mfma_f32_16x16x32_f16 v[74:77], v[42:45], v[18:21], v[74:77]
	s_waitcnt vmcnt(9)
	v_mfma_f32_16x16x32_f16 v[18:21], v[46:49], v[18:21], v[50:53]
	s_waitcnt lgkmcnt(2)
	v_mfma_f32_16x16x32_f16 v[50:53], v[34:37], v[22:25], v[78:81]
	v_mfma_f32_16x16x32_f16 v[78:81], v[38:41], v[22:25], v[82:85]
	v_mfma_f32_16x16x32_f16 v[82:85], v[42:45], v[22:25], v[86:89]
	v_mfma_f32_16x16x32_f16 v[22:25], v[46:49], v[22:25], v[54:57]
	s_waitcnt lgkmcnt(1)
	v_mfma_f32_16x16x32_f16 v[54:57], v[34:37], v[26:29], v[90:93]
	v_mfma_f32_16x16x32_f16 v[86:89], v[38:41], v[26:29], v[94:97]
	v_mfma_f32_16x16x32_f16 v[90:93], v[42:45], v[26:29], v[98:101]
	v_mfma_f32_16x16x32_f16 v[26:29], v[46:49], v[26:29], v[58:61]
	s_waitcnt lgkmcnt(0)
	v_mfma_f32_16x16x32_f16 v[58:61], v[34:37], v[30:33], v[102:105]
	v_mfma_f32_16x16x32_f16 v[94:97], v[38:41], v[30:33], v[106:109]
	v_mfma_f32_16x16x32_f16 v[98:101], v[42:45], v[30:33], v[110:113]
	v_mfma_f32_16x16x32_f16 v[30:33], v[46:49], v[30:33], v[62:65]
	s_setprio 0
	s_nop 1
	v_add_u32_e32 v62, 0x10000, v163
	v_add_u32_e32 v102, 0x14000, v163
	v_add_u32_e32 v106, 0x18000, v163
	v_add_u32_e32 v110, 0x1c000, v163
	ds_read_b128 v[62:65], v62
	ds_read_b128 v[102:105], v102
	ds_read_b128 v[106:109], v106
	ds_read_b128 v[110:113], v110
	s_setprio 1
	s_waitcnt lgkmcnt(3)
	v_mfma_f32_16x16x32_f16 v[130:133], v[34:37], v[62:65], v[130:133]
	v_mfma_f32_16x16x32_f16 v[134:137], v[38:41], v[62:65], v[134:137]
	v_mfma_f32_16x16x32_f16 v[138:141], v[42:45], v[62:65], v[138:141]
	v_mfma_f32_16x16x32_f16 v[62:65], v[46:49], v[62:65], v[114:117]
	s_waitcnt lgkmcnt(2)
	v_mfma_f32_16x16x32_f16 v[114:117], v[34:37], v[102:105], v[142:145]
	v_mfma_f32_16x16x32_f16 v[142:145], v[38:41], v[102:105], v[146:149]
	v_mfma_f32_16x16x32_f16 v[146:149], v[42:45], v[102:105], v[150:153]
	v_mfma_f32_16x16x32_f16 v[102:105], v[46:49], v[102:105], v[118:121]
	s_waitcnt lgkmcnt(1)
	v_mfma_f32_16x16x32_f16 v[118:121], v[34:37], v[106:109], v[154:157]
	v_mfma_f32_16x16x32_f16 v[150:153], v[38:41], v[106:109], v[158:161]
	v_mfma_f32_16x16x32_f16 v[154:157], v[42:45], v[106:109], v[170:173]
	v_mfma_f32_16x16x32_f16 v[106:109], v[46:49], v[106:109], v[122:125]
	s_waitcnt lgkmcnt(0)
	v_mfma_f32_16x16x32_f16 v[34:37], v[34:37], v[110:113], v[2:5]
	v_mfma_f32_16x16x32_f16 v[38:41], v[38:41], v[110:113], v[6:9]
	v_mfma_f32_16x16x32_f16 v[42:45], v[42:45], v[110:113], v[10:13]
	v_mfma_f32_16x16x32_f16 v[46:49], v[46:49], v[110:113], v[14:17]
	s_setprio 0
	s_xor_b32 s2, s58, 1
	s_lshl_b32 s49, s2, 3
	s_or_b32 s51, s49, s50
	s_lshl_b32 s0, s51, 12
	v_lshl_add_u64 v[14:15], v[166:167], 0, s[0:1]
	s_waitcnt vmcnt(8)
	s_barrier
	v_lshlrev_b32_e32 v255, 4, v0
	v_readfirstlane_b32 s92, v0
	s_lshl_b32 s92, s92, 4
	s_xor_b32 s93, s58, 1
	s_lshl_b32 s94, s93, 13
	s_add_i32 s92, s92, s94
	s_lshl_b32 s94, s34, 3
	s_or_b32 s94, s94, s33
	s_xor_b32 s94, s94, 1
	s_lshl_b32 s94, s94, 16
	s_add_u32 s88, s26, s94
	s_addc_u32 s89, s27, 0
	s_add_i32 s95, s92, 0x0
	s_mov_b32 m0, s95
	s_add_u32 s84, s88, 0x0
	s_addc_u32 s85, s89, 0
	global_load_lds_dwordx4 v255, s[84:85] sc0 sc1
	s_add_i32 s95, s92, 0x4000
	s_mov_b32 m0, s95
	s_add_u32 s84, s88, 0x2000
	s_addc_u32 s85, s89, 0
	global_load_lds_dwordx4 v255, s[84:85] sc0 sc1
	s_add_i32 s95, s92, 0x8000
	s_mov_b32 m0, s95
	s_add_u32 s84, s88, 0x4000
	s_addc_u32 s85, s89, 0
	global_load_lds_dwordx4 v255, s[84:85] sc0 sc1
	s_add_i32 s95, s92, 0xc000
	s_mov_b32 m0, s95
	s_add_u32 s84, s88, 0x6000
	s_addc_u32 s85, s89, 0
	global_load_lds_dwordx4 v255, s[84:85] sc0 sc1
	s_add_i32 s95, s92, 0x10000
	s_mov_b32 m0, s95
	s_add_u32 s84, s88, 0x8000
	s_addc_u32 s85, s89, 0
	global_load_lds_dwordx4 v255, s[84:85] sc0 sc1
	s_add_i32 s95, s92, 0x14000
	s_mov_b32 m0, s95
	s_add_u32 s84, s88, 0xa000
	s_addc_u32 s85, s89, 0
	global_load_lds_dwordx4 v255, s[84:85] sc0 sc1
	s_add_i32 s95, s92, 0x18000
	s_mov_b32 m0, s95
	s_add_u32 s84, s88, 0xc000
	s_addc_u32 s85, s89, 0
	global_load_lds_dwordx4 v255, s[84:85] sc0 sc1
	s_add_i32 s95, s92, 0x1c000
	s_mov_b32 m0, s95
	s_add_u32 s84, s88, 0xe000
	s_addc_u32 s85, s89, 0
	global_load_lds_dwordx4 v255, s[84:85] sc0 sc1
	global_load_dwordx4 v[2:5], v[14:15], off
	global_load_dwordx4 v[6:9], v[14:15], off offset:1024
	global_load_dwordx4 v[10:13], v[14:15], off offset:2048
	s_nop 0
	global_load_dwordx4 v[14:17], v[14:15], off offset:3072
	v_lshl_add_u32 v163, s52, 10, v191
	ds_read_b128 v[110:113], v163
	ds_read_b128 v[122:125], v163 offset:16384
	ds_read_b128 v[158:161], v163 offset:32768
	ds_read_b128 v[170:173], v163 offset:49152
	s_setprio 1
	s_waitcnt vmcnt(19) lgkmcnt(3)
	v_mfma_f32_16x16x32_f16 v[66:69], v[126:129], v[110:113], v[66:69]
	s_waitcnt vmcnt(18)
	v_mfma_f32_16x16x32_f16 v[70:73], v[174:177], v[110:113], v[70:73]
	s_waitcnt vmcnt(17)
	v_mfma_f32_16x16x32_f16 v[74:77], v[192:195], v[110:113], v[74:77]
	s_waitcnt vmcnt(16)
	v_mfma_f32_16x16x32_f16 v[110:113], v[196:199], v[110:113], v[18:21]
	s_waitcnt lgkmcnt(2)
	v_mfma_f32_16x16x32_f16 v[50:53], v[126:129], v[122:125], v[50:53]
	v_mfma_f32_16x16x32_f16 v[78:81], v[174:177], v[122:125], v[78:81]
	v_mfma_f32_16x16x32_f16 v[82:85], v[192:195], v[122:125], v[82:85]
	v_mfma_f32_16x16x32_f16 v[122:125], v[196:199], v[122:125], v[22:25]
	s_waitcnt lgkmcnt(1)
	v_mfma_f32_16x16x32_f16 v[216:219], v[126:129], v[158:161], v[54:57]
	v_mfma_f32_16x16x32_f16 v[86:89], v[174:177], v[158:161], v[86:89]
	v_mfma_f32_16x16x32_f16 v[90:93], v[192:195], v[158:161], v[90:93]
	v_mfma_f32_16x16x32_f16 v[158:161], v[196:199], v[158:161], v[26:29]
	s_waitcnt lgkmcnt(0)
	v_mfma_f32_16x16x32_f16 v[94:97], v[174:177], v[170:173], v[94:97]
	v_mfma_f32_16x16x32_f16 v[98:101], v[192:195], v[170:173], v[98:101]
	v_mfma_f32_16x16x32_f16 v[220:223], v[126:129], v[170:173], v[58:61]
	v_mfma_f32_16x16x32_f16 v[170:173], v[196:199], v[170:173], v[30:33]
	s_setprio 0
	v_add_u32_e32 v18, 0x10000, v163
	v_add_u32_e32 v22, 0x14000, v163
	v_add_u32_e32 v26, 0x18000, v163
	v_add_u32_e32 v30, 0x1c000, v163
	ds_read_b128 v[18:21], v18
	ds_read_b128 v[22:25], v22
	ds_read_b128 v[26:29], v26
	ds_read_b128 v[30:33], v30
	s_setprio 1
	s_waitcnt lgkmcnt(3)
	v_mfma_f32_16x16x32_f16 v[130:133], v[126:129], v[18:21], v[130:133]
	v_mfma_f32_16x16x32_f16 v[134:137], v[174:177], v[18:21], v[134:137]
	v_mfma_f32_16x16x32_f16 v[138:141], v[192:195], v[18:21], v[138:141]
	s_waitcnt lgkmcnt(2)
	v_mfma_f32_16x16x32_f16 v[114:117], v[126:129], v[22:25], v[114:117]
	v_mfma_f32_16x16x32_f16 v[142:145], v[174:177], v[22:25], v[142:145]
	v_mfma_f32_16x16x32_f16 v[146:149], v[192:195], v[22:25], v[146:149]
	s_waitcnt lgkmcnt(1)
	v_mfma_f32_16x16x32_f16 v[150:153], v[174:177], v[26:29], v[150:153]
	v_mfma_f32_16x16x32_f16 v[154:157], v[192:195], v[26:29], v[154:157]
	v_mfma_f32_16x16x32_f16 v[224:227], v[196:199], v[18:21], v[62:65]
	v_mfma_f32_16x16x32_f16 v[228:231], v[196:199], v[22:25], v[102:105]
	v_mfma_f32_16x16x32_f16 v[232:235], v[126:129], v[26:29], v[118:121]
	v_mfma_f32_16x16x32_f16 v[236:239], v[196:199], v[26:29], v[106:109]
	s_waitcnt lgkmcnt(0)
	v_mfma_f32_16x16x32_f16 v[240:243], v[126:129], v[30:33], v[34:37]
	v_mfma_f32_16x16x32_f16 v[174:177], v[174:177], v[30:33], v[38:41]
	v_mfma_f32_16x16x32_f16 v[192:195], v[192:195], v[30:33], v[42:45]
	v_mfma_f32_16x16x32_f16 v[196:199], v[196:199], v[30:33], v[46:49]
	s_setprio 0
	s_or_b32 s52, s49, s24
	s_lshl_b32 s0, s52, 12
	v_lshl_add_u64 v[30:31], v[166:167], 0, s[0:1]
	global_load_dwordx4 v[18:21], v[30:31], off
	global_load_dwordx4 v[22:25], v[30:31], off offset:1024
	global_load_dwordx4 v[26:29], v[30:31], off offset:2048
	s_nop 0
	global_load_dwordx4 v[30:33], v[30:31], off offset:3072
	v_lshl_add_u32 v118, s25, 10, v191
	ds_read_b128 v[46:49], v118
	ds_read_b128 v[62:65], v118 offset:16384
	ds_read_b128 v[102:105], v118 offset:32768
	ds_read_b128 v[106:109], v118 offset:49152
	s_setprio 1
	s_waitcnt vmcnt(19) lgkmcnt(3)
	v_mfma_f32_16x16x32_f16 v[34:37], v[200:203], v[46:49], v[66:69]
	s_waitcnt vmcnt(18)
	v_mfma_f32_16x16x32_f16 v[38:41], v[204:207], v[46:49], v[70:73]
	s_waitcnt vmcnt(17)
	v_mfma_f32_16x16x32_f16 v[42:45], v[208:211], v[46:49], v[74:77]
	s_waitcnt vmcnt(16)
	v_mfma_f32_16x16x32_f16 v[46:49], v[212:215], v[46:49], v[110:113]
	s_waitcnt lgkmcnt(2)
	v_mfma_f32_16x16x32_f16 v[50:53], v[200:203], v[62:65], v[50:53]
	v_mfma_f32_16x16x32_f16 v[54:57], v[204:207], v[62:65], v[78:81]
	v_mfma_f32_16x16x32_f16 v[58:61], v[208:211], v[62:65], v[82:85]
	v_mfma_f32_16x16x32_f16 v[62:65], v[212:215], v[62:65], v[122:125]
	s_waitcnt lgkmcnt(1)
	v_mfma_f32_16x16x32_f16 v[66:69], v[200:203], v[102:105], v[216:219]
	v_mfma_f32_16x16x32_f16 v[70:73], v[204:207], v[102:105], v[86:89]
	v_mfma_f32_16x16x32_f16 v[74:77], v[208:211], v[102:105], v[90:93]
	v_mfma_f32_16x16x32_f16 v[78:81], v[212:215], v[102:105], v[158:161]
	s_waitcnt lgkmcnt(0)
	v_mfma_f32_16x16x32_f16 v[82:85], v[200:203], v[106:109], v[220:223]
	v_mfma_f32_16x16x32_f16 v[86:89], v[204:207], v[106:109], v[94:97]
	v_mfma_f32_16x16x32_f16 v[90:93], v[208:211], v[106:109], v[98:101]
	v_mfma_f32_16x16x32_f16 v[94:97], v[212:215], v[106:109], v[170:173]
	s_setprio 0
	s_nop 0
	v_add_u32_e32 v98, 0x10000, v118
	v_add_u32_e32 v99, 0x14000, v118
	ds_read_b128 v[110:113], v98
	ds_read_b128 v[126:129], v99
	v_add_u32_e32 v98, 0x18000, v118
	v_add_u32_e32 v99, 0x1c000, v118
	ds_read_b128 v[158:161], v98
	ds_read_b128 v[170:173], v99
	s_setprio 1
	s_waitcnt lgkmcnt(3)
	v_mfma_f32_16x16x32_f16 v[98:101], v[200:203], v[110:113], v[130:133]
	v_mfma_f32_16x16x32_f16 v[102:105], v[204:207], v[110:113], v[134:137]
	v_mfma_f32_16x16x32_f16 v[106:109], v[208:211], v[110:113], v[138:141]
	v_mfma_f32_16x16x32_f16 v[110:113], v[212:215], v[110:113], v[224:227]
	s_waitcnt lgkmcnt(2)
	v_mfma_f32_16x16x32_f16 v[114:117], v[200:203], v[126:129], v[114:117]
	v_mfma_f32_16x16x32_f16 v[118:121], v[204:207], v[126:129], v[142:145]
	v_mfma_f32_16x16x32_f16 v[122:125], v[208:211], v[126:129], v[146:149]
	v_mfma_f32_16x16x32_f16 v[126:129], v[212:215], v[126:129], v[228:231]
	s_waitcnt lgkmcnt(1)
	v_mfma_f32_16x16x32_f16 v[130:133], v[200:203], v[158:161], v[232:235]
	v_mfma_f32_16x16x32_f16 v[134:137], v[204:207], v[158:161], v[150:153]
	v_mfma_f32_16x16x32_f16 v[138:141], v[208:211], v[158:161], v[154:157]
	v_mfma_f32_16x16x32_f16 v[142:145], v[212:215], v[158:161], v[236:239]
	s_waitcnt lgkmcnt(0)
	v_mfma_f32_16x16x32_f16 v[146:149], v[200:203], v[170:173], v[240:243]
	v_mfma_f32_16x16x32_f16 v[150:153], v[204:207], v[170:173], v[174:177]
	v_mfma_f32_16x16x32_f16 v[154:157], v[208:211], v[170:173], v[192:195]
	v_mfma_f32_16x16x32_f16 v[158:161], v[212:215], v[170:173], v[196:199]
	s_setprio 0
	s_waitcnt vmcnt(0)
	s_barrier
	s_getreg_b32 s24, hwreg(HW_REG_XCC_ID, 0, 4)
	s_and_saveexec_b64 s[0:1], s[4:5]
	s_cbranch_execz .LBB5_145
	s_and_b32 s53, s24, 15
	s_lshl_b32 s24, s34, 3
	s_or_b32 s50, s24, s50
	s_or_b32 s24, s50, s58
	s_lshl_b32 s24, s24, 5
	s_ashr_i32 s25, s24, 31
	s_lshl_b64 s[24:25], s[24:25], 2
	s_add_u32 s24, s46, s24
	s_addc_u32 s25, s47, s25
	s_add_i32 s54, s53, 1
	v_mov_b32_e32 v163, s54
	s_or_b32 s24, s50, s2
	s_lshl_b32 s24, s24, 5
	s_ashr_i32 s25, s24, 31
	s_lshl_b64 s[24:25], s[24:25], 2
	s_add_u32 s24, s46, s24
	s_addc_u32 s25, s47, s25
	s_mov_b32 s90, 0
	v_mov_b32_e32 v163, v254
	v_cmp_ne_u32_e32 vcc, 0, v163
	s_cbranch_vccnz .LBB5_144
	s_mov_b32 s90, 2
	v_mov_b32_e32 v165, 0
